# projection GEMM (panel-local order): column-tile sequence rotated by (panel & 3) so the 32 workgroups of an XCD work on 4 different weight tiles / output column blocks at a time
# speedup vs baseline: 1.0651x; 1.0087x over previous
.LBB0_479:
	v_readlane_b32 s5, v254, 42
	s_cmp_lg_u32 s5, 0
	s_cbranch_scc0 .Lrot_skip
	s_and_b32 s4, s93, 3

.LBB0_490:
	s_andn2_b64 vcc, exec, s[2:3]
	s_cbranch_vccnz .LBB0_494
	s_cmp_ge_u32 s93, s39
	s_mov_b64 s[24:25], 0
	s_cbranch_scc1 .LBB0_493
	s_mov_b64 s[24:25], -1
	s_mov_b32 s23, s44
	s_and_b32 s5, s44, 3
	s_add_i32 s5, s5, s93
	s_cmp_ge_u32 s5, s39
	s_cbranch_scc0 .Lrot_nowrap
	s_sub_i32 s5, s5, s39
.Lrot_nowrap:
.LBB0_493:
	s_mov_b32 s52, s5
	s_mov_b32 s22, s23
